# v089 with the VALU-writes-VCC to VALU-reads-VCC wait states (s_nop 1) added in the chunk-ranking code; otherwise identical
# speedup vs baseline: 1.0004x; 1.0004x over previous
.LBB1_141:
	s_or_b64 exec, exec, s[6:7]
	v_and_b32_e32 v1, 31, v0
	s_waitcnt lgkmcnt(0)
	v_lshlrev_b32_e32 v2, 2, v1
	v_or_b32_e32 v22, 32, v8
	s_barrier
	v_readfirstlane_b32 s95, v9
	v_min_u32_e32 v24, 8, v1
	v_mov_b32_e32 v25, 0x12810
	v_lshl_add_u32 v25, v24, 10, v25
	ds_read_b32 v25, v25
	v_mov_b32_e32 v27, 0
	s_waitcnt lgkmcnt(0)
	v_mov_b32_e32 v26, v25
	s_nop 1
	v_mov_b32_dpp v26, v25 row_shl:1 row_mask:0xf bank_mask:0xf
	v_sub_u32_e32 v26, v26, v25
	v_lshl_or_b32 v26, v26, 3, v24
	s_nop 1
	v_readlane_b32 s86, v26, 0
	v_readlane_b32 s87, v26, 1
	v_readlane_b32 s88, v26, 2
	v_readlane_b32 s89, v26, 3
	v_readlane_b32 s90, v26, 4
	v_readlane_b32 s91, v26, 5
	v_readlane_b32 s92, v26, 6
	v_readlane_b32 s93, v26, 7
	v_cmp_lt_u32_e32 vcc, s86, v26
	s_nop 1
	v_addc_co_u32_e32 v27, vcc, 0, v27, vcc
	v_cmp_lt_u32_e32 vcc, s87, v26
	s_nop 1
	v_addc_co_u32_e32 v27, vcc, 0, v27, vcc
	v_cmp_lt_u32_e32 vcc, s88, v26
	s_nop 1
	v_addc_co_u32_e32 v27, vcc, 0, v27, vcc
	v_cmp_lt_u32_e32 vcc, s89, v26
	s_nop 1
	v_addc_co_u32_e32 v27, vcc, 0, v27, vcc
	v_cmp_lt_u32_e32 vcc, s90, v26
	s_nop 1
	v_addc_co_u32_e32 v27, vcc, 0, v27, vcc
	v_cmp_lt_u32_e32 vcc, s91, v26
	s_nop 1
	v_addc_co_u32_e32 v27, vcc, 0, v27, vcc
	v_cmp_lt_u32_e32 vcc, s92, v26
	s_nop 1
	v_addc_co_u32_e32 v27, vcc, 0, v27, vcc
	v_cmp_lt_u32_e32 vcc, s93, v26
	s_nop 1
	v_addc_co_u32_e32 v27, vcc, 0, v27, vcc
	v_sub_u32_e32 v24, 11, v27
	v_cmp_gt_u32_e32 vcc, 4, v27
	s_nop 1
	v_cndmask_b32_e32 v27, v24, v27, vcc
	v_cmp_eq_u32_e32 vcc, s95, v27
	s_nop 0
	s_ff1_i32_b64 s95, vcc
	v_mov_b32_e32 v9, s95
	s_lshl_b32 s84, s95, 3
	s_add_u32 s85, s84, 8
	v_lshlrev_b32_e32 v3, 2, v22
	s_waitcnt vmcnt(0)
	v_mov_b32_e32 v18, v108
	v_mov_b32_e32 v19, v109
	v_mov_b32_e32 v20, v110
	v_mov_b32_e32 v16, v111
	v_mov_b32_e32 v17, v112
	v_mov_b32_e32 v12, v113
	v_mov_b32_e32 v13, v114
	v_mov_b32_e32 v15, v115
	v_mov_b32_e32 v4, 0x180
	v_lshl_or_b32 v23, v8, 2, v4
	v_mov_b32_e32 v21, v116
	v_mov_b32_e32 v4, v117
	v_mov_b32_e32 v5, v118
	v_mov_b32_e32 v10, v119
	v_mov_b32_e32 v3, 0x12810
	v_lshl_add_u32 v23, v9, 10, v3
	ds_read2_b32 v[24:25], v23 offset1:32
	v_add_u32_e32 v2, v23, v2
	ds_read2_b32 v[230:231], v2 offset1:1
	v_lshlrev_b32_e32 v26, 8, v9
	s_lshl_b32 s2, s2, 11
	v_or3_b32 v235, v26, s2, v1
	s_mov_b32 s12, 0x7a120
	s_waitcnt lgkmcnt(1)
	v_readfirstlane_b32 s13, v24
	v_readfirstlane_b32 s6, v25
	v_cmp_gt_i32_e32 vcc, s12, v235
	v_mov_b32_e32 v2, 0
	v_mov_b32_e32 v238, 0
	s_and_saveexec_b64 s[2:3], vcc
	s_cbranch_execz .LBB1_143
	v_ashrrev_i32_e32 v25, 31, v235
	v_mov_b32_e32 v24, v235
	v_lshl_add_u64 v[24:25], v[24:25], 2, s[50:51]
	global_load_dword v238, v[24:25], off
